# DSA attention steady loop: selection mask enters the QK^T MFMA as C operand (0/-inf) read from a 256 B LDS table by 4-bit groups instead of 2 VALU ops per element; numerics identical
# speedup vs baseline: 1.2746x; 1.0164x over previous
.LBB0_1066:
	s_andn2_b64 vcc, exec, s[0:1]
	s_cbranch_vccnz .LBB0_1165
	v_readlane_b32 s0, v250, 19
	v_readlane_b32 s1, v250, 20
	s_andn2_b64 vcc, exec, s[0:1]
	s_cbranch_vccnz .LBB0_1165
	s_add_u32 s0, s74, 0x7800000
	v_writelane_b32 v253, s0, 47
	s_addc_u32 s0, s75, 0
	v_writelane_b32 v253, s0, 49
	s_add_u32 s0, s74, 0xa800000
	v_writelane_b32 v253, s0, 50
	s_addc_u32 s0, s75, 0
	v_writelane_b32 v253, s0, 52
	s_add_u32 s0, s74, 0xb800000
	v_writelane_b32 v253, s0, 53
	s_addc_u32 s0, s75, 0
	s_waitcnt vmcnt(0) lgkmcnt(0)
	v_lshrrev_b32_e32 v3, 5, v198
	v_lshlrev_b32_e32 v4, 1, v235
	v_writelane_b32 v253, s0, 55
	s_add_u32 s0, s74, 0xeb00000
	v_and_b32_e32 v6, 32, v4
	v_lshlrev_b32_e32 v238, 2, v3
	v_lshrrev_b32_e32 v4, 2, v235
	s_addc_u32 s82, s75, 0
	v_and_b32_e32 v236, 31, v235
	v_and_or_b32 v4, v4, 3, v238
	v_writelane_b32 v253, s0, 57
	s_add_u32 s83, s74, 0xf0000
	v_lshlrev_b32_e32 v5, 3, v235
	v_lshlrev_b32_e32 v7, 6, v4
	v_lshlrev_b32_e32 v8, 4, v236
	v_lshlrev_b32_e32 v4, 9, v236
	s_addc_u32 s84, s75, 0
	v_and_b32_e32 v2, 24, v5
	v_lshl_or_b32 v4, v3, 3, v4
	v_lshl_or_b32 v241, v3, 10, v8
	v_lshlrev_b32_e32 v242, 9, v3
	v_lshrrev_b32_e32 v3, 3, v198
	v_readlane_b32 s0, v253, 4
	v_or3_b32 v239, v6, v2, v7
	v_and_b32_e32 v6, 56, v5
	v_or_b32_e32 v5, 8, v3
	s_add_u32 s85, s0, s86
	v_readlane_b32 s0, v253, 5
	v_lshlrev_b32_e32 v243, 7, v3
	v_lshlrev_b32_e32 v8, 9, v3
	v_lshlrev_b32_e32 v244, 7, v5
	v_lshlrev_b32_e32 v10, 9, v5
	v_or_b32_e32 v5, 16, v3
	v_or_b32_e32 v3, 24, v3
	s_addc_u32 s88, s0, s87
	v_readlane_b32 s0, v253, 6
	v_lshlrev_b32_e32 v0, 9, v198
	v_lshlrev_b32_e32 v12, 9, v5
	v_lshlrev_b32_e32 v14, 9, v3
	s_add_u32 s89, s0, s86
	v_readlane_b32 s0, v253, 7
	v_lshrrev_b32_e32 v237, 2, v198
	v_or_b32_e32 v240, 0x6000, v239
	v_cmp_gt_u32_e64 s[36:37], 32, v198
	v_lshlrev_b32_e32 v245, 7, v5
	v_lshlrev_b32_e32 v246, 7, v3
	s_addc_u32 s90, s0, s87
	v_lshlrev_b32_e32 v200, 1, v0
	v_lshlrev_b32_e32 v202, 1, v2
	v_lshlrev_b32_e32 v247, 1, v4
	v_lshlrev_b32_e32 v204, 1, v6
	v_lshlrev_b32_e32 v206, 1, v8
	v_lshlrev_b32_e32 v208, 1, v10
	v_lshlrev_b32_e32 v210, 1, v12
	v_lshlrev_b32_e32 v212, 1, v14
	v_readlane_b32 s91, v250, 9
	s_mov_b32 s100, 0x15000
	v_lshrrev_b32_e32 v226, 2, v198
	v_and_b32_e32 v227, 3, v198
	v_lshrrev_b32_e32 v226, v227, v226
	v_and_b32_e32 v226, 1, v226
	v_cmp_eq_u32_e32 vcc, 1, v226
	v_mov_b32_e32 v226, 0xff800000
	s_nop 1
	v_cndmask_b32_e64 v226, v226, 0, vcc
	v_lshlrev_b32_e32 v227, 2, v198
	v_add_u32_e32 v227, s100, v227
	ds_write_b32 v227, v226
	s_waitcnt lgkmcnt(0)
	s_branch .LBB0_1070

.LBB0_1077:
	v_lshl_add_u64 v[14:15], v[184:185], 0, s[54:55]
	s_mov_b32 s38, 0xeb20000
	v_add_co_u32_e32 v2, vcc, s38, v14
	s_mov_b32 s38, 0xeb28000
	s_nop 0
	v_addc_co_u32_e32 v3, vcc, 0, v15, vcc
	v_add_co_u32_e32 v4, vcc, s38, v14
	v_add_u32_e32 v12, s29, v239
	s_nop 0
	v_addc_co_u32_e32 v5, vcc, 0, v15, vcc
	global_load_dword v0, v[2:3], off
	global_load_dword v190, v[4:5], off
	global_load_dword v191, v[182:183], off offset:-4
	v_lshrrev_b32_e32 v2, v238, v211
	v_lshrrev_b32_e32 v3, v238, v213
	v_bfe_u32 v4, v2, 0, 4
	v_lshl_add_u32 v4, v4, 4, s100
	ds_read_b128 v[80:83], v4
	v_bfe_u32 v4, v2, 8, 4
	v_lshl_add_u32 v4, v4, 4, s100
	ds_read_b128 v[84:87], v4
	v_bfe_u32 v4, v2, 16, 4
	v_lshl_add_u32 v4, v4, 4, s100
	ds_read_b128 v[88:91], v4
	v_bfe_u32 v4, v2, 24, 4
	v_lshl_add_u32 v4, v4, 4, s100
	ds_read_b128 v[92:95], v4
	v_bfe_u32 v4, v3, 0, 4
	v_lshl_add_u32 v4, v4, 4, s100
	ds_read_b128 v[96:99], v4
	v_bfe_u32 v4, v3, 8, 4
	v_lshl_add_u32 v4, v4, 4, s100
	ds_read_b128 v[100:103], v4
	v_bfe_u32 v4, v3, 16, 4
	v_lshl_add_u32 v4, v4, 4, s100
	ds_read_b128 v[104:107], v4
	v_bfe_u32 v4, v3, 24, 4
	v_lshl_add_u32 v4, v4, 4, s100
	ds_read_b128 v[108:111], v4
	ds_read_b64_tr_b16 v[176:177], v12 offset:24576
	ds_read_b64_tr_b16 v[178:179], v12 offset:25088
	s_waitcnt lgkmcnt(6)
	v_mfma_f32_32x32x16_bf16 v[80:95], v[172:175], v[124:127], v[80:95]
	v_add_f32_e32 v2, v64, v65
	v_add_f32_e32 v2, v66, v2
	v_add_f32_e32 v2, v67, v2
	v_add_f32_e32 v2, v68, v2
	v_add_f32_e32 v2, v69, v2
	v_cvt_pk_bf16_f32 v140, v64, v65
	v_cvt_pk_bf16_f32 v141, v66, v67
	ds_read_b64_tr_b16 v[172:173], v12 offset:28672
	ds_read_b64_tr_b16 v[174:175], v12 offset:29184
	s_waitcnt lgkmcnt(4)
	v_mfma_f32_32x32x16_bf16 v[96:111], v[164:167], v[124:127], v[96:111]
	v_add_f32_e32 v2, v70, v2
	v_add_f32_e32 v2, v71, v2
	v_add_f32_e32 v2, v72, v2
	v_add_f32_e32 v2, v73, v2
	v_cvt_pk_bf16_f32 v142, v68, v69
	v_cvt_pk_bf16_f32 v143, v70, v71
	ds_read_b64_tr_b16 v[164:165], v12 offset:25600
	ds_read_b64_tr_b16 v[166:167], v12 offset:26112
	s_waitcnt lgkmcnt(11)
	v_mfma_f32_32x32x16_bf16 v[80:95], v[168:171], v[120:123], v[80:95]
	v_add_f32_e32 v2, v74, v2
	v_add_f32_e32 v2, v75, v2
	v_add_f32_e32 v2, v76, v2
	v_add_f32_e32 v2, v77, v2
	v_cvt_pk_bf16_f32 v136, v72, v73
	v_cvt_pk_bf16_f32 v137, v74, v75
	ds_read_b64_tr_b16 v[168:169], v12 offset:29696
	ds_read_b64_tr_b16 v[170:171], v12 offset:30208
	s_waitcnt lgkmcnt(12)
	v_mfma_f32_32x32x16_bf16 v[96:111], v[160:163], v[120:123], v[96:111]
	v_add_f32_e32 v2, v78, v2
	v_add_f32_e32 v2, v79, v2
	v_add_f32_e32 v2, v48, v2
	v_add_f32_e32 v2, v49, v2
	v_cvt_pk_bf16_f32 v138, v76, v77
	v_cvt_pk_bf16_f32 v139, v78, v79
	ds_read_b64_tr_b16 v[160:161], v12 offset:26624
	ds_read_b64_tr_b16 v[162:163], v12 offset:27136
	s_waitcnt lgkmcnt(13)
	v_mfma_f32_32x32x16_bf16 v[80:95], v[156:159], v[116:119], v[80:95]
	v_add_f32_e32 v2, v50, v2
	v_add_f32_e32 v2, v51, v2
	v_add_f32_e32 v2, v52, v2
	v_add_f32_e32 v6, v53, v2
	v_cvt_pk_bf16_f32 v132, v48, v49
	v_cvt_pk_bf16_f32 v133, v50, v51
	ds_read_b64_tr_b16 v[2:3], v12 offset:30720
	ds_read_b64_tr_b16 v[4:5], v12 offset:31232
	s_waitcnt lgkmcnt(14)
	v_mfma_f32_32x32x16_bf16 v[96:111], v[152:155], v[116:119], v[96:111]
	v_add_f32_e32 v6, v54, v6
	v_add_f32_e32 v6, v55, v6
	v_add_f32_e32 v6, v56, v6
	v_add_f32_e32 v10, v57, v6
	v_cvt_pk_bf16_f32 v134, v52, v53
	v_cvt_pk_bf16_f32 v135, v54, v55
	ds_read_b64_tr_b16 v[6:7], v12 offset:27648
	ds_read_b64_tr_b16 v[8:9], v12 offset:28160
	s_waitcnt lgkmcnt(14)
	v_mfma_f32_32x32x16_bf16 v[80:95], v[148:151], v[112:115], v[80:95]
	v_add_f32_e32 v10, v58, v10
	v_add_f32_e32 v10, v59, v10
	v_add_f32_e32 v10, v60, v10
	v_add_f32_e32 v48, v61, v10
	v_cvt_pk_bf16_f32 v128, v56, v57
	v_cvt_pk_bf16_f32 v129, v58, v59
	ds_read_b64_tr_b16 v[10:11], v12 offset:31744
	ds_read_b64_tr_b16 v[12:13], v12 offset:32256
	v_mfma_f32_32x32x16_bf16 v[96:111], v[144:147], v[112:115], v[96:111]
	v_add_f32_e32 v48, v62, v48
	v_add_f32_e32 v48, v63, v48
	v_add_f32_e32 v48, 0, v48
	v_cvt_pk_bf16_f32 v130, v60, v61
	v_cvt_pk_bf16_f32 v131, v62, v63
	v_lshl_add_u64 v[186:187], v[216:217], 0, s[54:55]
	v_lshl_add_u64 v[50:51], v[186:187], 0, s[20:21]
	s_add_i32 s29, s59, s63
	s_mov_b32 s38, m0
	s_mov_b32 m0, s29
	s_nop 0
	global_load_lds_dwordx4 v[50:51], off
	s_mov_b32 m0, s38
	v_lshl_add_u64 v[188:189], v[218:219], 0, s[54:55]
	v_lshl_add_u64 v[50:51], v[188:189], 0, s[24:25]
	s_add_i32 s29, s57, s62
	s_mov_b32 s38, m0
	s_mov_b32 m0, s29
	s_nop 0
	global_load_lds_dwordx4 v[50:51], off
	s_mov_b32 m0, s38
	s_waitcnt vmcnt(7)
	v_mul_f32_e32 v49, v201, v209
	v_cmp_nge_f32_e32 vcc, s73, v49
	v_cmp_neq_f32_e64 s[38:39], 0, v207
	s_or_b64 vcc, vcc, s[38:39]
	v_cndmask_b32_e64 v49, 0, 1, vcc
	v_cmp_ne_u32_e64 s[38:39], 0, v49
	s_cmp_lg_u64 s[38:39], 0
	s_cselect_b64 s[38:39], -1, 0
	s_cbranch_vccz .LBB0_1079
	v_sub_f32_e32 v95, v95, v207
	v_sub_f32_e32 v94, v94, v207
	v_sub_f32_e32 v93, v93, v207
	v_sub_f32_e32 v92, v92, v207
	v_sub_f32_e32 v91, v91, v207
	v_sub_f32_e32 v90, v90, v207
	v_sub_f32_e32 v89, v89, v207
	v_sub_f32_e32 v88, v88, v207
	v_sub_f32_e32 v87, v87, v207
	v_sub_f32_e32 v86, v86, v207
	v_sub_f32_e32 v85, v85, v207
	v_sub_f32_e32 v84, v84, v207
	v_sub_f32_e32 v83, v83, v207
	v_sub_f32_e32 v82, v82, v207
	v_sub_f32_e32 v81, v81, v207
	v_sub_f32_e32 v80, v80, v207
	v_sub_f32_e32 v111, v111, v207
	v_sub_f32_e32 v110, v110, v207
	v_sub_f32_e32 v109, v109, v207
	v_sub_f32_e32 v108, v108, v207
	v_sub_f32_e32 v107, v107, v207
	v_sub_f32_e32 v106, v106, v207
	v_sub_f32_e32 v105, v105, v207
	v_sub_f32_e32 v104, v104, v207
	v_sub_f32_e32 v103, v103, v207
	v_sub_f32_e32 v102, v102, v207
	v_sub_f32_e32 v101, v101, v207
	v_sub_f32_e32 v100, v100, v207
	v_sub_f32_e32 v99, v99, v207
	v_sub_f32_e32 v98, v98, v207
	v_sub_f32_e32 v97, v97, v207
	v_sub_f32_e32 v96, v96, v207
.LBB0_1079:
	v_add_f32_e32 v193, v248, v48
	s_andn2_b64 vcc, exec, s[38:39]
	s_mov_b64 s[40:41], 0
	s_cbranch_vccz .Lslow_in_A
.LBB0_1080:
	s_waitcnt lgkmcnt(14)
	v_mfma_f32_32x32x16_bf16 v[32:47], v[140:143], v[176:179], v[32:47]
	v_exp_f32_e32 v64, v80
	v_exp_f32_e32 v65, v81
	v_exp_f32_e32 v66, v82
	v_exp_f32_e32 v67, v83
	s_waitcnt lgkmcnt(12)
	v_mfma_f32_32x32x16_bf16 v[16:31], v[140:143], v[172:175], v[16:31]
	v_exp_f32_e32 v68, v84
	v_exp_f32_e32 v69, v85
	v_exp_f32_e32 v70, v86
	v_exp_f32_e32 v71, v87
	v_add_u32_e32 v84, s57, v241
	ds_read_b128 v[140:143], v84
	ds_read_b128 v[148:151], v84 offset:2048
	s_waitcnt lgkmcnt(12)
	v_mfma_f32_32x32x16_bf16 v[32:47], v[136:139], v[164:167], v[32:47]
	v_exp_f32_e32 v72, v88
	v_exp_f32_e32 v73, v89
	v_exp_f32_e32 v74, v90
	v_exp_f32_e32 v75, v91
	ds_read_b128 v[176:179], v84 offset:2560
	ds_read_b128 v[172:175], v84 offset:4096
	s_waitcnt lgkmcnt(12)
	v_mfma_f32_32x32x16_bf16 v[16:31], v[136:139], v[168:171], v[16:31]
	v_exp_f32_e32 v76, v92
	v_exp_f32_e32 v77, v93
	v_exp_f32_e32 v78, v94
	v_exp_f32_e32 v79, v95
	ds_read_b128 v[136:139], v84 offset:512
	ds_read_b128 v[164:167], v84 offset:4608
	s_waitcnt lgkmcnt(12)
	v_mfma_f32_32x32x16_bf16 v[32:47], v[132:135], v[160:163], v[32:47]
	v_exp_f32_e32 v48, v96
	v_exp_f32_e32 v49, v97
	v_exp_f32_e32 v50, v98
	v_exp_f32_e32 v51, v99
	ds_read_b128 v[168:171], v84 offset:6144
	ds_read_b128 v[160:163], v84 offset:6656
	s_waitcnt lgkmcnt(12)
	v_mfma_f32_32x32x16_bf16 v[16:31], v[132:135], v[2:5], v[16:31]
	v_exp_f32_e32 v52, v100
	v_exp_f32_e32 v53, v101
	v_exp_f32_e32 v54, v102
	v_exp_f32_e32 v55, v103
	s_waitcnt lgkmcnt(10)
	v_mfma_f32_32x32x16_bf16 v[32:47], v[128:131], v[6:9], v[32:47]
	v_exp_f32_e32 v56, v104
	v_exp_f32_e32 v57, v105
	v_exp_f32_e32 v58, v106
	v_exp_f32_e32 v59, v107
	s_waitcnt lgkmcnt(8)
	v_mfma_f32_32x32x16_bf16 v[16:31], v[128:131], v[10:13], v[16:31]
	v_exp_f32_e32 v60, v108
	v_exp_f32_e32 v61, v109
	v_exp_f32_e32 v62, v110
	v_exp_f32_e32 v63, v111
	s_waitcnt vmcnt(2) lgkmcnt(0)
	s_barrier
	s_andn2_b64 vcc, exec, s[40:41]
	s_cbranch_vccnz .LBB0_1082
	s_waitcnt lgkmcnt(0)
	ds_read_b128 v[2:5], v203 offset:49248
	ds_read_b128 v[6:9], v203 offset:49216
	ds_read_b128 v[10:13], v203 offset:49184
	ds_read_b128 v[84:87], v203 offset:49152
	s_waitcnt lgkmcnt(3)
	v_pk_mul_f32 v[46:47], v[46:47], v[4:5]
	s_waitcnt lgkmcnt(2)
	v_pk_mul_f32 v[42:43], v[42:43], v[8:9]
	s_waitcnt lgkmcnt(1)
	v_pk_mul_f32 v[38:39], v[38:39], v[12:13]
	s_waitcnt lgkmcnt(0)
	v_pk_mul_f32 v[34:35], v[34:35], v[86:87]
	v_pk_mul_f32 v[44:45], v[44:45], v[2:3]
	v_pk_mul_f32 v[40:41], v[40:41], v[6:7]
	v_pk_mul_f32 v[36:37], v[36:37], v[10:11]
	v_pk_mul_f32 v[32:33], v[32:33], v[84:85]
	v_pk_mul_f32 v[30:31], v[30:31], v[4:5]
	v_pk_mul_f32 v[26:27], v[26:27], v[8:9]
	v_pk_mul_f32 v[22:23], v[22:23], v[12:13]
	v_pk_mul_f32 v[18:19], v[18:19], v[86:87]
	v_pk_mul_f32 v[28:29], v[28:29], v[2:3]
	v_pk_mul_f32 v[24:25], v[24:25], v[6:7]
	v_pk_mul_f32 v[20:21], v[20:21], v[10:11]
	v_pk_mul_f32 v[16:17], v[16:17], v[84:85]
.LBB0_1082:
	s_add_i32 s29, s57, 0x2000
	s_cmpk_lg_i32 s57, 0x4000
	s_cselect_b32 s65, s29, 0
	v_add_co_u32_e32 v2, vcc, 0xeb30000, v14
	v_add_u32_e32 v12, s59, v239
	s_nop 0
	v_addc_co_u32_e32 v3, vcc, 0, v15, vcc
	global_load_dword v192, v[2:3], off
	v_add_co_u32_e32 v2, vcc, 0xeb38000, v14
	s_nop 1
	v_addc_co_u32_e32 v3, vcc, 0, v15, vcc
	global_load_dword v14, v[2:3], off
	global_load_dword v209, v[182:183], off
	v_lshrrev_b32_e32 v2, v238, v0
	v_lshrrev_b32_e32 v3, v238, v190
	v_bfe_u32 v4, v2, 0, 4
	v_lshl_add_u32 v4, v4, 4, s100
	ds_read_b128 v[80:83], v4
	v_bfe_u32 v4, v2, 8, 4
	v_lshl_add_u32 v4, v4, 4, s100
	ds_read_b128 v[84:87], v4
	v_bfe_u32 v4, v2, 16, 4
	v_lshl_add_u32 v4, v4, 4, s100
	ds_read_b128 v[88:91], v4
	v_bfe_u32 v4, v2, 24, 4
	v_lshl_add_u32 v4, v4, 4, s100
	ds_read_b128 v[92:95], v4
	v_bfe_u32 v4, v3, 0, 4
	v_lshl_add_u32 v4, v4, 4, s100
	ds_read_b128 v[96:99], v4
	v_bfe_u32 v4, v3, 8, 4
	v_lshl_add_u32 v4, v4, 4, s100
	ds_read_b128 v[100:103], v4
	v_bfe_u32 v4, v3, 16, 4
	v_lshl_add_u32 v4, v4, 4, s100
	ds_read_b128 v[104:107], v4
	v_bfe_u32 v4, v3, 24, 4
	v_lshl_add_u32 v4, v4, 4, s100
	ds_read_b128 v[108:111], v4
	ds_read_b64_tr_b16 v[156:157], v12 offset:24576
	ds_read_b64_tr_b16 v[158:159], v12 offset:25088
	s_waitcnt lgkmcnt(6)
	v_mfma_f32_32x32x16_bf16 v[80:95], v[140:143], v[124:127], v[80:95]
	v_add_f32_e32 v2, v64, v65
	v_add_f32_e32 v2, v66, v2
	v_add_f32_e32 v2, v67, v2
	v_add_f32_e32 v2, v68, v2
	v_add_f32_e32 v2, v69, v2
	v_cvt_pk_bf16_f32 v140, v64, v65
	v_cvt_pk_bf16_f32 v141, v66, v67
	ds_read_b64_tr_b16 v[152:153], v12 offset:28672
	ds_read_b64_tr_b16 v[154:155], v12 offset:29184
	s_waitcnt lgkmcnt(4)
	v_mfma_f32_32x32x16_bf16 v[96:111], v[136:139], v[124:127], v[96:111]
	v_add_f32_e32 v2, v70, v2
	v_add_f32_e32 v2, v71, v2
	v_add_f32_e32 v2, v72, v2
	v_add_f32_e32 v2, v73, v2
	v_cvt_pk_bf16_f32 v142, v68, v69
	v_cvt_pk_bf16_f32 v143, v70, v71
	ds_read_b64_tr_b16 v[144:145], v12 offset:25600
	ds_read_b64_tr_b16 v[146:147], v12 offset:26112
	s_waitcnt lgkmcnt(11)
	v_mfma_f32_32x32x16_bf16 v[80:95], v[148:151], v[120:123], v[80:95]
	v_add_f32_e32 v2, v74, v2
	v_add_f32_e32 v2, v75, v2
	v_add_f32_e32 v2, v76, v2
	v_add_f32_e32 v2, v77, v2
	v_cvt_pk_bf16_f32 v136, v72, v73
	v_cvt_pk_bf16_f32 v137, v74, v75
	ds_read_b64_tr_b16 v[148:149], v12 offset:29696
	ds_read_b64_tr_b16 v[150:151], v12 offset:30208
	s_waitcnt lgkmcnt(12)
	v_mfma_f32_32x32x16_bf16 v[96:111], v[176:179], v[120:123], v[96:111]
	v_add_f32_e32 v2, v78, v2
	v_add_f32_e32 v2, v79, v2
	v_add_f32_e32 v2, v48, v2
	v_add_f32_e32 v2, v49, v2
	v_cvt_pk_bf16_f32 v138, v76, v77
	v_cvt_pk_bf16_f32 v139, v78, v79
	ds_read_b64_tr_b16 v[176:177], v12 offset:26624
	ds_read_b64_tr_b16 v[178:179], v12 offset:27136
	s_waitcnt lgkmcnt(13)
	v_mfma_f32_32x32x16_bf16 v[80:95], v[172:175], v[116:119], v[80:95]
	v_add_f32_e32 v2, v50, v2
	v_add_f32_e32 v2, v51, v2
	v_add_f32_e32 v2, v52, v2
	v_add_f32_e32 v6, v53, v2
	v_cvt_pk_bf16_f32 v132, v48, v49
	v_cvt_pk_bf16_f32 v133, v50, v51
	ds_read_b64_tr_b16 v[2:3], v12 offset:30720
	ds_read_b64_tr_b16 v[4:5], v12 offset:31232
	s_waitcnt lgkmcnt(14)
	v_mfma_f32_32x32x16_bf16 v[96:111], v[164:167], v[116:119], v[96:111]
	v_add_f32_e32 v6, v54, v6
	v_add_f32_e32 v6, v55, v6
	v_add_f32_e32 v6, v56, v6
	v_add_f32_e32 v10, v57, v6
	v_cvt_pk_bf16_f32 v134, v52, v53
	v_cvt_pk_bf16_f32 v135, v54, v55
	ds_read_b64_tr_b16 v[6:7], v12 offset:27648
	ds_read_b64_tr_b16 v[8:9], v12 offset:28160
	s_waitcnt lgkmcnt(14)
	v_mfma_f32_32x32x16_bf16 v[80:95], v[168:171], v[112:115], v[80:95]
	v_add_f32_e32 v10, v58, v10
	v_add_f32_e32 v10, v59, v10
	v_add_f32_e32 v10, v60, v10
	v_add_f32_e32 v15, v61, v10
	v_cvt_pk_bf16_f32 v128, v56, v57
	v_cvt_pk_bf16_f32 v129, v58, v59
	ds_read_b64_tr_b16 v[10:11], v12 offset:31744
	ds_read_b64_tr_b16 v[12:13], v12 offset:32256
	v_mfma_f32_32x32x16_bf16 v[96:111], v[160:163], v[112:115], v[96:111]
	v_add_f32_e32 v15, v62, v15
	v_add_f32_e32 v15, v63, v15
	v_add_f32_e32 v15, 0, v15
	v_cvt_pk_bf16_f32 v130, v60, v61
	v_cvt_pk_bf16_f32 v131, v62, v63
	v_lshl_add_u64 v[48:49], v[186:187], 0, s[22:23]
	s_add_i32 s29, s57, s63
	s_mov_b32 s38, m0
	s_mov_b32 m0, s29
	s_nop 0
	global_load_lds_dwordx4 v[48:49], off
	s_mov_b32 m0, s38
	v_lshl_add_u64 v[48:49], v[188:189], 0, s[70:71]
	s_add_i32 s29, s65, s62
	s_mov_b32 s38, m0
	s_mov_b32 m0, s29
	s_nop 0
	global_load_lds_dwordx4 v[48:49], off
	s_mov_b32 m0, s38
	s_waitcnt vmcnt(7)
	v_mul_f32_e32 v48, v201, v191
	v_cmp_nge_f32_e32 vcc, s73, v48
	v_cmp_neq_f32_e64 s[38:39], 0, v207
	s_or_b64 vcc, vcc, s[38:39]
	v_cndmask_b32_e64 v48, 0, 1, vcc
	v_cmp_ne_u32_e64 s[38:39], 0, v48
	s_cmp_lg_u64 s[38:39], 0
	s_cselect_b64 s[38:39], -1, 0
	s_cbranch_vccz .LBB0_1084
	v_sub_f32_e32 v95, v95, v207
	v_sub_f32_e32 v94, v94, v207
	v_sub_f32_e32 v93, v93, v207
	v_sub_f32_e32 v92, v92, v207
	v_sub_f32_e32 v91, v91, v207
	v_sub_f32_e32 v90, v90, v207
	v_sub_f32_e32 v89, v89, v207
	v_sub_f32_e32 v88, v88, v207
	v_sub_f32_e32 v87, v87, v207
	v_sub_f32_e32 v86, v86, v207
	v_sub_f32_e32 v85, v85, v207
	v_sub_f32_e32 v84, v84, v207
	v_sub_f32_e32 v83, v83, v207
	v_sub_f32_e32 v82, v82, v207
	v_sub_f32_e32 v81, v81, v207
	v_sub_f32_e32 v80, v80, v207
	v_sub_f32_e32 v111, v111, v207
	v_sub_f32_e32 v110, v110, v207
	v_sub_f32_e32 v109, v109, v207
	v_sub_f32_e32 v108, v108, v207
	v_sub_f32_e32 v107, v107, v207
	v_sub_f32_e32 v106, v106, v207
	v_sub_f32_e32 v105, v105, v207
	v_sub_f32_e32 v104, v104, v207
	v_sub_f32_e32 v103, v103, v207
	v_sub_f32_e32 v102, v102, v207
	v_sub_f32_e32 v101, v101, v207
	v_sub_f32_e32 v100, v100, v207
	v_sub_f32_e32 v99, v99, v207
	v_sub_f32_e32 v98, v98, v207
	v_sub_f32_e32 v97, v97, v207
	v_sub_f32_e32 v96, v96, v207
.LBB0_1084:
	v_add_f32_e32 v248, v193, v15
	v_or_b32_e32 v15, v213, v211
	v_cmp_ne_u32_e32 vcc, 0, v15
	s_nop 3
	s_or_b64 s[42:43], s[42:43], vcc
	s_andn2_b64 vcc, exec, s[38:39]
	s_mov_b64 s[40:41], 0
	s_cbranch_vccz .Lslow_in_B
.LBB0_1085:
	s_waitcnt lgkmcnt(14)
	v_mfma_f32_32x32x16_bf16 v[32:47], v[140:143], v[156:159], v[32:47]
	v_exp_f32_e32 v64, v80
	v_exp_f32_e32 v65, v81
	v_exp_f32_e32 v66, v82
	v_exp_f32_e32 v67, v83
	s_waitcnt lgkmcnt(12)
	v_mfma_f32_32x32x16_bf16 v[16:31], v[140:143], v[152:155], v[16:31]
	v_exp_f32_e32 v68, v84
	v_exp_f32_e32 v69, v85
	v_exp_f32_e32 v70, v86
	v_exp_f32_e32 v71, v87
	v_add_u32_e32 v80, s65, v241
	ds_read_b128 v[172:175], v80
	ds_read_b128 v[164:167], v80 offset:512
	s_waitcnt lgkmcnt(12)
	v_mfma_f32_32x32x16_bf16 v[32:47], v[136:139], v[144:147], v[32:47]
	v_exp_f32_e32 v72, v88
	v_exp_f32_e32 v73, v89
	v_exp_f32_e32 v74, v90
	v_exp_f32_e32 v75, v91
	ds_read_b128 v[168:171], v80 offset:2048
	ds_read_b128 v[160:163], v80 offset:2560
	s_waitcnt lgkmcnt(12)
	v_mfma_f32_32x32x16_bf16 v[16:31], v[136:139], v[148:151], v[16:31]
	v_exp_f32_e32 v76, v92
	v_exp_f32_e32 v77, v93
	v_exp_f32_e32 v78, v94
	v_exp_f32_e32 v79, v95
	ds_read_b128 v[156:159], v80 offset:4096
	ds_read_b128 v[152:155], v80 offset:4608
	s_waitcnt lgkmcnt(12)
	v_mfma_f32_32x32x16_bf16 v[32:47], v[132:135], v[176:179], v[32:47]
	v_exp_f32_e32 v48, v96
	v_exp_f32_e32 v49, v97
	v_exp_f32_e32 v50, v98
	v_exp_f32_e32 v51, v99
	ds_read_b128 v[148:151], v80 offset:6144
	ds_read_b128 v[144:147], v80 offset:6656
	s_waitcnt lgkmcnt(12)
	v_mfma_f32_32x32x16_bf16 v[16:31], v[132:135], v[2:5], v[16:31]
	v_exp_f32_e32 v52, v100
	v_exp_f32_e32 v53, v101
	v_exp_f32_e32 v54, v102
	v_exp_f32_e32 v55, v103
	s_waitcnt lgkmcnt(10)
	v_mfma_f32_32x32x16_bf16 v[32:47], v[128:131], v[6:9], v[32:47]
	v_exp_f32_e32 v56, v104
	v_exp_f32_e32 v57, v105
	v_exp_f32_e32 v58, v106
	v_exp_f32_e32 v59, v107
	s_waitcnt lgkmcnt(8)
	v_mfma_f32_32x32x16_bf16 v[16:31], v[128:131], v[10:13], v[16:31]
	v_exp_f32_e32 v60, v108
	v_exp_f32_e32 v61, v109
	v_exp_f32_e32 v62, v110
	v_exp_f32_e32 v63, v111
	s_waitcnt vmcnt(2) lgkmcnt(0)
	s_barrier
	s_andn2_b64 vcc, exec, s[40:41]
	s_cbranch_vccnz .LBB0_1087
	s_waitcnt lgkmcnt(0)
	ds_read_b128 v[2:5], v203 offset:49248
	ds_read_b128 v[6:9], v203 offset:49216
	ds_read_b128 v[10:13], v203 offset:49184
	ds_read_b128 v[80:83], v203 offset:49152
	s_waitcnt lgkmcnt(3)
	v_pk_mul_f32 v[46:47], v[46:47], v[4:5]
	s_waitcnt lgkmcnt(2)
	v_pk_mul_f32 v[42:43], v[42:43], v[8:9]
	s_waitcnt lgkmcnt(1)
	v_pk_mul_f32 v[38:39], v[38:39], v[12:13]
	s_waitcnt lgkmcnt(0)
	v_pk_mul_f32 v[34:35], v[34:35], v[82:83]
	v_pk_mul_f32 v[44:45], v[44:45], v[2:3]
	v_pk_mul_f32 v[40:41], v[40:41], v[6:7]
	v_pk_mul_f32 v[36:37], v[36:37], v[10:11]
	v_pk_mul_f32 v[32:33], v[32:33], v[80:81]
	v_pk_mul_f32 v[30:31], v[30:31], v[4:5]
	v_pk_mul_f32 v[26:27], v[26:27], v[8:9]
	v_pk_mul_f32 v[22:23], v[22:23], v[12:13]
	v_pk_mul_f32 v[18:19], v[18:19], v[82:83]
	v_pk_mul_f32 v[28:29], v[28:29], v[2:3]
	v_pk_mul_f32 v[24:25], v[24:25], v[6:7]
	v_pk_mul_f32 v[20:21], v[20:21], v[10:11]
	v_pk_mul_f32 v[16:17], v[16:17], v[80:81]

.Lslow_in_A:
	v_mov_b32_e32 v64, v80
	v_mov_b32_e32 v65, v81
	v_mov_b32_e32 v66, v82
	v_mov_b32_e32 v67, v83
	v_mov_b32_e32 v68, v84
	v_mov_b32_e32 v69, v85
	v_mov_b32_e32 v70, v86
	v_mov_b32_e32 v71, v87
	v_mov_b32_e32 v72, v88
	v_mov_b32_e32 v73, v89
	v_mov_b32_e32 v74, v90
	v_mov_b32_e32 v75, v91
	v_mov_b32_e32 v76, v92
	v_mov_b32_e32 v77, v93
	v_mov_b32_e32 v78, v94
	v_mov_b32_e32 v79, v95
	v_mov_b32_e32 v48, v96
	v_mov_b32_e32 v49, v97
	v_mov_b32_e32 v50, v98
	v_mov_b32_e32 v51, v99
	v_mov_b32_e32 v52, v100
	v_mov_b32_e32 v53, v101
	v_mov_b32_e32 v54, v102
	v_mov_b32_e32 v55, v103
	v_mov_b32_e32 v56, v104
	v_mov_b32_e32 v57, v105
	v_mov_b32_e32 v58, v106
	v_mov_b32_e32 v59, v107
	v_mov_b32_e32 v60, v108
	v_mov_b32_e32 v61, v109
	v_mov_b32_e32 v62, v110
	v_mov_b32_e32 v63, v111
	s_branch .LBB0_1089
.Lslow_out_A:
	v_mov_b32_e32 v80, v64
	v_mov_b32_e32 v81, v65
	v_mov_b32_e32 v82, v66
	v_mov_b32_e32 v83, v67
	v_mov_b32_e32 v84, v68
	v_mov_b32_e32 v85, v69
	v_mov_b32_e32 v86, v70
	v_mov_b32_e32 v87, v71
	v_mov_b32_e32 v88, v72
	v_mov_b32_e32 v89, v73
	v_mov_b32_e32 v90, v74
	v_mov_b32_e32 v91, v75
	v_mov_b32_e32 v92, v76
	v_mov_b32_e32 v93, v77
	v_mov_b32_e32 v94, v78
	v_mov_b32_e32 v95, v79
	v_mov_b32_e32 v96, v48
	v_mov_b32_e32 v97, v49
	v_mov_b32_e32 v98, v50
	v_mov_b32_e32 v99, v51
	v_mov_b32_e32 v100, v52
	v_mov_b32_e32 v101, v53
	v_mov_b32_e32 v102, v54
	v_mov_b32_e32 v103, v55
	v_mov_b32_e32 v104, v56
	v_mov_b32_e32 v105, v57
	v_mov_b32_e32 v106, v58
	v_mov_b32_e32 v107, v59
	v_mov_b32_e32 v108, v60
	v_mov_b32_e32 v109, v61
	v_mov_b32_e32 v110, v62
	v_mov_b32_e32 v111, v63
	s_branch .LBB0_1080
.Lslow_in_B:
	v_mov_b32_e32 v48, v80
	v_mov_b32_e32 v65, v81
	v_mov_b32_e32 v66, v82
	v_mov_b32_e32 v67, v83
	v_mov_b32_e32 v68, v84
	v_mov_b32_e32 v69, v85
	v_mov_b32_e32 v70, v86
	v_mov_b32_e32 v71, v87
	v_mov_b32_e32 v72, v88
	v_mov_b32_e32 v73, v89
	v_mov_b32_e32 v74, v90
	v_mov_b32_e32 v75, v91
	v_mov_b32_e32 v76, v92
	v_mov_b32_e32 v77, v93
	v_mov_b32_e32 v78, v94
	v_mov_b32_e32 v79, v95
	v_mov_b32_e32 v15, v96
	v_mov_b32_e32 v49, v97
	v_mov_b32_e32 v50, v98
	v_mov_b32_e32 v51, v99
	v_mov_b32_e32 v52, v100
	v_mov_b32_e32 v53, v101
	v_mov_b32_e32 v54, v102
	v_mov_b32_e32 v55, v103
	v_mov_b32_e32 v56, v104
	v_mov_b32_e32 v57, v105
	v_mov_b32_e32 v58, v106
	v_mov_b32_e32 v59, v107
	v_mov_b32_e32 v60, v108
	v_mov_b32_e32 v61, v109
	v_mov_b32_e32 v62, v110
	v_mov_b32_e32 v63, v111
	s_branch .LBB0_1093
.Lslow_out_B:
	v_mov_b32_e32 v80, v48
	v_mov_b32_e32 v81, v65
	v_mov_b32_e32 v82, v66
	v_mov_b32_e32 v83, v67
	v_mov_b32_e32 v84, v68
	v_mov_b32_e32 v85, v69
	v_mov_b32_e32 v86, v70
	v_mov_b32_e32 v87, v71
	v_mov_b32_e32 v88, v72
	v_mov_b32_e32 v89, v73
	v_mov_b32_e32 v90, v74
	v_mov_b32_e32 v91, v75
	v_mov_b32_e32 v92, v76
	v_mov_b32_e32 v93, v77
	v_mov_b32_e32 v94, v78
	v_mov_b32_e32 v95, v79
	v_mov_b32_e32 v96, v15
	v_mov_b32_e32 v97, v49
	v_mov_b32_e32 v98, v50
	v_mov_b32_e32 v99, v51
	v_mov_b32_e32 v100, v52
	v_mov_b32_e32 v101, v53
	v_mov_b32_e32 v102, v54
	v_mov_b32_e32 v103, v55
	v_mov_b32_e32 v104, v56
	v_mov_b32_e32 v105, v57
	v_mov_b32_e32 v106, v58
	v_mov_b32_e32 v107, v59
	v_mov_b32_e32 v108, v60
	v_mov_b32_e32 v109, v61
	v_mov_b32_e32 v110, v62
	v_mov_b32_e32 v111, v63
	s_branch .LBB0_1085
